# v15 + 4096 more layer-1 expert copy items in the q|k|v tail (12288 there, 12288 in layer-1 router idle waves)
# baseline (speedup 1.0000x reference)
; #define LAS __attribute__((address_space(3)))
; template <class T> __device__ __forceinline__ T* wsp(const Frame& F, size_t off) { return (T*)(F.ws + off); }
;     LAS float* scr = (LAS float*)(F.lds + RING_OFF + F.wave * 16384);
;     const int gw = (ncu ? (int)blockIdx.x - cu0 : F.vcu) * NWAVES + F.wave, NGW = (ncu ? ncu : F.G) * NWAVES;
;     bf16* UP = wsp<bf16>(F, WS_WEUP); bf16* DN = wsp<bf16>(F, WS_WEDN);
;     for (int it = it0 + gw; it < it1; it += NGW) {
;         const int e = it / 384, r = it % 384; const size_t eo = (size_t)(layer * 64 + e) * 1024 * 256;
;         if (r < 128) p0_transpose_item(inp(F, I_WGATE) + eo, 1024, 256, UP + (size_t)e * 512 * 1024, 3, scr, r, F.lane);
;         else if (r < 256) p0_transpose_item(inp(F, I_WUP) + eo, 1024, 256, UP + (size_t)e * 512 * 1024, 4, scr, r - 128, F.lane);
;         else p0_transpose_item(inp(F, I_WDOWN) + eo, 256, 1024, DN + (size_t)e * 1024 * 256, 5, scr, r - 256, F.lane, 16.f);
;     }
; __global__ void __launch_bounds__(NWAVES * 64, 2) mega_fwd(Args args) {
;     ...
;         if (CVT_EARLY > 0 && F.G == 256 && bx >= 64) { FENCE(F); convert_experts(F, 1, 0, CVT_EARLY, 64, 192); }
.LBB0_1163:
	s_cmpk_lg_i32 s67, 0x100
	s_cselect_b64 s[0:1], -1, 0
	s_cmp_lt_i32 s8, 64
	s_cselect_b64 s[2:3], -1, 0
	s_or_b64 s[0:1], s[2:3], s[0:1]
	s_and_b64 vcc, exec, s[0:1]
	s_cbranch_vccnz .LBB0_1175
	v_mov_b32_e32 v2, v0
	s_lshl_b32 s0, s8, 3
	v_readfirstlane_b32 s1, v2
	s_ashr_i32 s1, s1, 6
	s_add_i32 s0, s0, s1
	s_add_i32 s9, s0, 0xfffffe00
	s_cmpk_gt_i32 s9, 0x2fff
	s_cbranch_scc1 .LBB0_1175
	s_add_u32 s1, s38, 0x4800000
	s_addc_u32 s16, s39, 0
	s_add_u32 s17, s38, 0x2800000
	v_and_b32_e32 v1, 56, v2
	v_lshlrev_b32_e32 v2, 2, v2
	s_addc_u32 s18, s39, 0
	v_and_b32_e32 v10, 28, v2
	s_lshl_b32 s19, s9, 6
	s_lshl_b32 s20, s9, 5
	s_lshl_b32 s21, s9, 3
	s_lshl_b32 s22, s9, 1
	s_add_i32 s23, 0, 0x202a8
	v_mov_b32_e32 v7, 0
	s_movk_i32 s40, 0x1000
	s_movk_i32 s41, 0x2000
	s_movk_i32 s42, 0x4000
	s_movk_i32 s43, 0x6000
	s_movk_i32 s44, 0x7000
	s_mov_b32 s0, 0x41800000
	s_movk_i32 s45, 0x7fff
	s_mov_b32 s46, 0xffff0000
	s_mov_b64 s[2:3], 0x600
	s_add_i32 s47, 0, 0x202a0
	s_add_i32 s48, 0, 0x20298
	v_mov_b32_e32 v11, 1
	v_mov_b32_e32 v12, 0x400
	v_mov_b32_e32 v13, 0x7c
	s_branch .LBB0_1167
.LBB0_1166:
	s_add_i32 s4, s9, 0x600
	s_add_i32 s19, s19, 0x18000
	s_add_i32 s20, s20, 0xc000
	s_addk_i32 s21, 0x3000
	s_addk_i32 s22, 0xc00
	s_cmpk_lt_i32 s9, 0x2a00
	s_mov_b32 s9, s4
	s_waitcnt lgkmcnt(0)
	global_store_dwordx4 v[8:9], v[2:5], off nt
	s_cbranch_scc0 .LBB0_1175

; #define LAS __attribute__((address_space(3)))
; template <class T> __device__ __forceinline__ T* wsp(const Frame& F, size_t off) { return (T*)(F.ws + off); }
;     LAS float* scr = (LAS float*)(F.lds + RING_OFF + F.wave * 16384);
;     const int gw = (ncu ? (int)blockIdx.x - cu0 : F.vcu) * NWAVES + F.wave, NGW = (ncu ? ncu : F.G) * NWAVES;
;     bf16* UP = wsp<bf16>(F, WS_WEUP); bf16* DN = wsp<bf16>(F, WS_WEDN);
;     for (int it = it0 + gw; it < it1; it += NGW) {
;         const int e = it / 384, r = it % 384; const size_t eo = (size_t)(layer * 64 + e) * 1024 * 256;
;         if (r < 128) p0_transpose_item(inp(F, I_WGATE) + eo, 1024, 256, UP + (size_t)e * 512 * 1024, 3, scr, r, F.lane);
;         else if (r < 256) p0_transpose_item(inp(F, I_WUP) + eo, 1024, 256, UP + (size_t)e * 512 * 1024, 4, scr, r - 128, F.lane);
;         else p0_transpose_item(inp(F, I_WDOWN) + eo, 256, 1024, DN + (size_t)e * 1024 * 256, 5, scr, r - 256, F.lane, 16.f);
.Lcv1_entry:
	s_cmpk_lg_i32 s67, 0x100
	s_cbranch_scc1 .Lcv1_end
	v_mov_b32_e32 v2, v0
	s_mul_i32 s4, s71, 6
	s_movk_i32 s2, 0x600
	v_readfirstlane_b32 s5, v2
	s_movk_i32 s3, 0x2000
	s_ashr_i32 s5, s5, 6
	s_add_i32 s5, s5, s4
	s_addk_i32 s5, 0x2ffe
	s_cmpk_gt_i32 s5, 0x5fff
	s_cbranch_scc1 .Lcv1_end
	s_add_u32 s9, s38, 0x4800000
	s_addc_u32 s18, s39, 0
	s_add_u32 s19, s38, 0x2800000
	v_and_b32_e32 v1, 56, v2
	v_lshlrev_b32_e32 v2, 2, v2
	s_addc_u32 s20, s39, 0
	v_and_b32_e32 v10, 28, v2
	s_lshl_b32 s21, s5, 6
	s_lshl_b32 s22, s2, 6
	s_lshl_b32 s23, s5, 5
	s_lshl_b32 s40, s2, 5
	s_lshl_b32 s41, s5, 3
	s_lshl_b32 s42, s2, 3
	s_lshl_b32 s43, s5, 1
	s_lshl_b32 s44, s2, 1
	s_add_i32 s45, 0, 0x202a8
	s_waitcnt lgkmcnt(1)
	v_mov_b32_e32 v7, 0
	s_movk_i32 s46, 0x1000
	s_movk_i32 s47, 0x4000
	s_movk_i32 s48, 0x6000
	s_movk_i32 s49, 0x7000
	s_mov_b32 s4, 0x41800000
	s_movk_i32 s50, 0x7fff
	s_mov_b32 s51, 0xffff0000
	s_mov_b64 s[10:11], 0x600
	s_add_i32 s52, 0, 0x202a0
	s_add_i32 s53, 0, 0x20298
	v_mov_b32_e32 v11, 1
	v_mov_b32_e32 v12, 0x400
	v_mov_b32_e32 v13, 0x7c
	s_branch .Lcv1_07
